# tailD + XCD-local unit order for grouped GEMMs
# speedup vs baseline: 1.0411x; 1.0019x over previous
; #define LAS __attribute__((address_space(3)))
; __device__ __forceinline__ void gu_mfma(const Args& a, LAS unsigned char* lds, int layer) {
;     seg_to_lds(a, lds, layer);
;     const LAS int* seg = (const LAS int*)(lds + SEG_OFF);
;     pg8::GroupedOrder So{(const char*)(a.ws + WS_HS), (const char*)(a.ws + WS_WGU + (size_t)layer * NE * 1024 * D * 2), seg, 4, (int)gridDim.x, (int)blockIdx.x, (size_t)D * 2, (size_t)1024 * D * 2, (size_t)256 * D * 2};
;     EpiGU E{(bf16_t*)(a.ws + WS_HID), seg};
;     pg8::gemm_phase_gather<EpiGU, pg8::GroupedOrder>(lds, D, So, E, (const char*)(a.ws + WS_ACT), (const int*)(a.ws + WS_LIST), seg);
.LBB0_898:
	s_or_b64 exec, exec, s[36:37]
	s_nop 1
	v_writelane_b32 v254, s61, 61
	s_nop 1
	s_and_b32 vcc_lo, s61, 7
	s_lshl_b32 vcc_lo, vcc_lo, 2
	s_lshr_b32 vcc_hi, s61, 3
	s_and_b32 vcc_hi, vcc_hi, 3
	s_or_b32 vcc_lo, vcc_lo, vcc_hi
	s_andn2_b32 s61, s61, 31
	s_or_b32 s61, s61, vcc_lo
	s_add_u32 vcc_lo, s61, s77
	s_nop 1
	v_writelane_b32 v253, vcc_lo, 31
	s_nop 1
